# speedup vs baseline: 1.0092x; 1.0081x over previous
_Z7k1_prepPKfPKiPiPfPDF16_S4_:
	s_load_dwordx2 s[4:5], s[0:1], 0x8
	s_cmp_gt_u32 s2, 63
	s_cbranch_scc1 .Lpf_skip
	v_cmp_gt_u32_e32 vcc, 64, v0
	s_and_saveexec_b64 s[68:69], vcc
	s_getpc_b64 s[70:71]
.Lpf_anchor:
	s_add_u32 s70, s70, .Lpf_k3code-.Lpf_anchor
	s_addc_u32 s71, s71, 0
	v_lshlrev_b32_e32 v70, 7, v0
	s_add_u32 s72, s70, 0x2000
	s_addc_u32 s73, s71, 0
	global_load_dword v71, v70, s[70:71]
	global_load_dword v71, v70, s[72:73]
	s_add_u32 s72, s70, 0x4000
	s_addc_u32 s73, s71, 0
	v_cmp_gt_u32_e32 vcc, 26, v0
	s_and_b64 exec, exec, vcc
	global_load_dword v71, v70, s[72:73]
	s_mov_b64 exec, s[68:69]
.Lpf_skip:
	v_mov_b32_e32 v39, 0
	v_lshlrev_b32_e32 v38, 4, v0
	s_movk_i32 s3, 0x2000
	v_and_b32_e32 v1, 63, v0
	s_waitcnt lgkmcnt(0)
	v_lshl_add_u64 v[18:19], s[4:5], 0, v[38:39]
	global_load_dwordx4 v[2:5], v38, s[4:5]
	v_add_co_u32_e32 v20, vcc, 0x1000, v18
	s_nop 1
	v_addc_co_u32_e32 v21, vcc, 0, v19, vcc
	global_load_dwordx4 v[22:25], v[20:21], off
	v_add_co_u32_e64 v6, s[4:5], s3, v18
	s_movk_i32 s3, 0x6000
	s_nop 0
	v_addc_co_u32_e64 v7, s[4:5], 0, v19, s[4:5]
	global_load_dwordx4 v[10:13], v[6:7], off
	v_add_co_u32_e32 v20, vcc, 0x3000, v18
	v_add_co_u32_e64 v30, s[4:5], s3, v18
	s_nop 0
	v_addc_co_u32_e32 v21, vcc, 0, v19, vcc
	v_addc_co_u32_e64 v31, s[4:5], 0, v19, s[4:5]
	s_movk_i32 s3, 0x7000
	global_load_dwordx4 v[26:29], v[20:21], off
	v_add_co_u32_e64 v14, s[4:5], s3, v18
	s_movk_i32 s3, 0x4000
	v_add_co_u32_e32 v18, vcc, s3, v18
	v_addc_co_u32_e64 v15, s[4:5], 0, v19, s[4:5]
	s_nop 0
	v_addc_co_u32_e32 v19, vcc, 0, v19, vcc
	global_load_dwordx4 v[14:17], v[14:15], off
	s_mov_b32 s3, 0x3f0000
	global_load_dwordx4 v[6:9], v[30:31], off offset:-4096
	v_cmp_eq_u32_e32 vcc, 0, v1
	global_load_dwordx4 v[18:21], v[18:19], off
	s_waitcnt vmcnt(6)
	v_mul_u32_u24_e32 v34, 6, v2
	global_load_dwordx4 v[30:33], v[30:31], off
	v_mul_u32_u24_e32 v36, 6, v3
	v_mul_u32_u24_e32 v40, 6, v4
	v_lshlrev_b64 v[34:35], v34, 1
	v_lshlrev_b64 v[36:37], v36, 1
	v_mul_u32_u24_e32 v42, 6, v5
	v_lshlrev_b64 v[40:41], v40, 1
	v_lshl_add_u64 v[34:35], v[34:35], 0, v[36:37]
	v_lshlrev_b64 v[42:43], v42, 1
	s_waitcnt vmcnt(6)
	v_mul_u32_u24_e32 v58, 6, v22
	v_lshl_add_u64 v[34:35], v[34:35], 0, v[40:41]
	v_mul_u32_u24_e32 v60, 6, v23
	v_lshlrev_b64 v[58:59], v58, 1
	v_lshl_add_u64 v[34:35], v[34:35], 0, v[42:43]
	v_mul_u32_u24_e32 v62, 6, v24
	v_lshlrev_b64 v[60:61], v60, 1
	v_lshl_add_u64 v[34:35], v[58:59], 0, v[34:35]
	v_mul_u32_u24_e32 v64, 6, v25
	v_lshlrev_b64 v[62:63], v62, 1
	v_lshl_add_u64 v[34:35], v[34:35], 0, v[60:61]
	s_waitcnt vmcnt(5)
	v_mul_u32_u24_e32 v36, 6, v10
	v_lshlrev_b64 v[64:65], v64, 1
	v_lshl_add_u64 v[34:35], v[34:35], 0, v[62:63]
	v_mul_u32_u24_e32 v44, 6, v11
	v_lshlrev_b64 v[36:37], v36, 1
	v_lshl_add_u64 v[34:35], v[34:35], 0, v[64:65]
	v_mul_u32_u24_e32 v45, 6, v12
	v_lshlrev_b64 v[40:41], v44, 1
	v_lshl_add_u64 v[34:35], v[36:37], 0, v[34:35]
	v_mul_u32_u24_e32 v46, 6, v13
	v_lshlrev_b64 v[44:45], v45, 1
	v_lshl_add_u64 v[34:35], v[34:35], 0, v[40:41]
	v_lshlrev_b64 v[46:47], v46, 1
	s_waitcnt vmcnt(4)
	v_mul_u32_u24_e32 v66, 6, v26
	v_lshl_add_u64 v[34:35], v[34:35], 0, v[44:45]
	v_mul_u32_u24_e32 v67, 6, v27
	v_lshlrev_b64 v[42:43], v66, 1
	v_lshl_add_u64 v[34:35], v[34:35], 0, v[46:47]
	v_mul_u32_u24_e32 v68, 6, v28
	v_lshlrev_b64 v[58:59], v67, 1
	v_lshl_add_u64 v[34:35], v[42:43], 0, v[34:35]
	v_mul_u32_u24_e32 v69, 6, v29
	v_lshlrev_b64 v[60:61], v68, 1
	v_lshl_add_u64 v[34:35], v[34:35], 0, v[58:59]
	v_lshlrev_b64 v[66:67], v69, 1
	v_lshl_add_u64 v[34:35], v[34:35], 0, v[60:61]
	s_waitcnt vmcnt(1)
	v_mul_u32_u24_e32 v44, 6, v18
	v_lshl_add_u64 v[34:35], v[34:35], 0, v[66:67]
	v_lshlrev_b64 v[44:45], v44, 1
	v_lshl_add_u64 v[34:35], v[44:45], 0, v[34:35]
	v_mul_u32_u24_e32 v44, 6, v19
	v_lshlrev_b64 v[44:45], v44, 1
	v_lshl_add_u64 v[34:35], v[34:35], 0, v[44:45]
	v_mul_u32_u24_e32 v44, 6, v20
	v_lshlrev_b64 v[44:45], v44, 1
	v_lshl_add_u64 v[34:35], v[34:35], 0, v[44:45]
	v_mul_u32_u24_e32 v44, 6, v21
	v_mul_u32_u24_e32 v48, 6, v6
	v_lshlrev_b64 v[44:45], v44, 1
	v_mul_u32_u24_e32 v56, 6, v7
	v_lshlrev_b64 v[48:49], v48, 1
	v_lshl_add_u64 v[34:35], v[34:35], 0, v[44:45]
	v_lshlrev_b64 v[56:57], v56, 1
	v_mul_u32_u24_e32 v36, 6, v8
	v_lshl_add_u64 v[34:35], v[48:49], 0, v[34:35]
	v_mul_u32_u24_e32 v50, 6, v9
	v_lshlrev_b64 v[36:37], v36, 1
	v_lshl_add_u64 v[34:35], v[34:35], 0, v[56:57]
	v_lshlrev_b64 v[50:51], v50, 1
	v_lshl_add_u64 v[34:35], v[34:35], 0, v[36:37]
	v_lshl_add_u64 v[34:35], v[34:35], 0, v[50:51]
	v_mul_u32_u24_e32 v52, 6, v14
	v_lshlrev_b64 v[52:53], v52, 1
	v_mul_u32_u24_e32 v40, 6, v15
	v_lshlrev_b64 v[40:41], v40, 1
	v_mul_u32_u24_e32 v42, 6, v16
	v_mul_u32_u24_e32 v54, 6, v17
	v_lshlrev_b64 v[42:43], v42, 1
	v_lshlrev_b64 v[54:55], v54, 1
	v_lshrrev_b32_e32 v44, 6, v0
	s_waitcnt vmcnt(0)
	v_mul_u32_u24_e32 v36, 6, v30
	v_lshlrev_b64 v[36:37], v36, 1
	v_lshl_add_u64 v[34:35], v[36:37], 0, v[34:35]
	v_mul_u32_u24_e32 v36, 6, v31
	v_lshlrev_b64 v[36:37], v36, 1
	v_lshl_add_u64 v[34:35], v[34:35], 0, v[36:37]
	v_mul_u32_u24_e32 v36, 6, v32
	v_lshlrev_b64 v[36:37], v36, 1
	v_lshl_add_u64 v[34:35], v[34:35], 0, v[36:37]
	v_mul_u32_u24_e32 v36, 6, v33
	v_lshlrev_b64 v[36:37], v36, 1
	v_lshl_add_u64 v[34:35], v[34:35], 0, v[36:37]
	v_lshl_add_u64 v[34:35], v[52:53], 0, v[34:35]
	v_lshl_add_u64 v[34:35], v[34:35], 0, v[40:41]
	v_lshl_add_u64 v[34:35], v[34:35], 0, v[42:43]
	v_lshl_add_u64 v[40:41], v[34:35], 0, v[54:55]
	v_lshlrev_b64 v[34:35], 20, v[40:41]
	v_and_b32_e32 v37, 63, v35
	v_lshlrev_b64 v[34:35], 30, v[40:41]
	v_and_b32_e32 v42, 0x3f0000, v35
	v_lshrrev_b64 v[34:35], 4, v[40:41]
	v_and_b32_e32 v45, 63, v35
	v_lshlrev_b64 v[34:35], 6, v[40:41]
	v_lshlrev_b32_e32 v36, 10, v40
	v_and_b32_e32 v34, 0x3f0000, v35
	v_and_b32_e32 v35, 63, v40
	v_and_or_b32 v35, v36, s3, v35
	v_or_b32_e32 v36, v37, v42
	v_bfe_u32 v37, v41, 16, 6
	v_add_u32_dpp v35, v35, v35 quad_perm:[1,0,3,2] row_mask:0xf bank_mask:0xf bound_ctrl:1
	v_lshrrev_b32_e32 v42, 6, v41
	v_alignbit_b32 v43, v41, v40, 14
	v_add_u32_dpp v35, v35, v35 quad_perm:[2,3,0,1] row_mask:0xf bank_mask:0xf bound_ctrl:1
	v_and_or_b32 v37, v42, s3, v37
	v_bfe_u32 v42, v40, 24, 6
	v_add_u32_dpp v35, v35, v35 row_half_mirror row_mask:0xf bank_mask:0xf bound_ctrl:1
	v_or_b32_e32 v34, v45, v34
	v_and_or_b32 v42, v43, s3, v42
	v_add_u32_dpp v35, v35, v35 row_mirror row_mask:0xf bank_mask:0xf bound_ctrl:1
	v_add_u32_dpp v34, v34, v34 quad_perm:[1,0,3,2] row_mask:0xf bank_mask:0xf bound_ctrl:1
	v_readlane_b32 s3, v35, 0
	v_readlane_b32 s6, v35, 16
	v_readlane_b32 s7, v35, 32
	v_readlane_b32 s8, v35, 48
	v_add_u32_dpp v35, v36, v36 quad_perm:[1,0,3,2] row_mask:0xf bank_mask:0xf bound_ctrl:1
	v_add_u32_dpp v34, v34, v34 quad_perm:[2,3,0,1] row_mask:0xf bank_mask:0xf bound_ctrl:1
	s_nop 0
	v_add_u32_dpp v35, v35, v35 quad_perm:[2,3,0,1] row_mask:0xf bank_mask:0xf bound_ctrl:1
	v_add_u32_dpp v34, v34, v34 row_half_mirror row_mask:0xf bank_mask:0xf bound_ctrl:1
	s_nop 0
	v_add_u32_dpp v35, v35, v35 row_half_mirror row_mask:0xf bank_mask:0xf bound_ctrl:1
	v_add_u32_dpp v34, v34, v34 row_mirror row_mask:0xf bank_mask:0xf bound_ctrl:1
	s_nop 0
	v_add_u32_dpp v35, v35, v35 row_mirror row_mask:0xf bank_mask:0xf bound_ctrl:1
	v_readlane_b32 s17, v34, 0
	v_readlane_b32 s10, v35, 0
	v_readlane_b32 s14, v35, 16
	v_readlane_b32 s15, v35, 32
	v_readlane_b32 s16, v35, 48
	v_add_u32_dpp v35, v42, v42 quad_perm:[1,0,3,2] row_mask:0xf bank_mask:0xf bound_ctrl:1
	v_readlane_b32 s18, v34, 16
	v_readlane_b32 s19, v34, 32
	v_readlane_b32 s20, v34, 48
	v_add_u32_dpp v34, v37, v37 quad_perm:[1,0,3,2] row_mask:0xf bank_mask:0xf bound_ctrl:1
	v_add_u32_dpp v35, v35, v35 quad_perm:[2,3,0,1] row_mask:0xf bank_mask:0xf bound_ctrl:1
	s_nop 0
	v_add_u32_dpp v34, v34, v34 quad_perm:[2,3,0,1] row_mask:0xf bank_mask:0xf bound_ctrl:1
	v_add_u32_dpp v35, v35, v35 row_half_mirror row_mask:0xf bank_mask:0xf bound_ctrl:1
	s_nop 0
	v_add_u32_dpp v34, v34, v34 row_half_mirror row_mask:0xf bank_mask:0xf bound_ctrl:1
	v_add_u32_dpp v35, v35, v35 row_mirror row_mask:0xf bank_mask:0xf bound_ctrl:1
	s_nop 0
	v_add_u32_dpp v34, v34, v34 row_mirror row_mask:0xf bank_mask:0xf bound_ctrl:1
	v_readlane_b32 s9, v35, 0
	v_readlane_b32 s11, v35, 16
	v_readlane_b32 s12, v35, 32
	v_readlane_b32 s13, v35, 48
	v_readlane_b32 s21, v34, 0
	v_readlane_b32 s22, v34, 16
	v_readlane_b32 s23, v34, 32
	v_readlane_b32 s24, v34, 48
	s_and_saveexec_b64 s[4:5], vcc
	s_cbranch_execz .LBB0_2
	s_add_i32 s3, s6, s3
	s_add_i32 s3, s3, s7
	s_add_i32 s10, s14, s10
	s_add_i32 s14, s3, s8
	s_add_i32 s3, s18, s17
	s_add_i32 s3, s3, s19
	s_add_i32 s7, s3, s20
	s_add_i32 s3, s11, s9
	s_add_i32 s3, s3, s12
	s_add_i32 s10, s10, s15
	s_add_i32 s6, s3, s13
	s_add_i32 s3, s22, s21
	v_mul_u32_u24_e32 v42, 24, v44
	s_add_i32 s15, s10, s16
	s_add_i32 s3, s3, s23
	v_or_b32_e32 v43, 0x5080, v42
	s_add_i32 s3, s3, s24
	v_mov_b64_e32 v[34:35], s[14:15]
	v_mov_b64_e32 v[36:37], s[6:7]
	v_mov_b32_e32 v46, s3
	v_mov_b32_e32 v47, v39
	ds_write2_b64 v43, v[34:35], v[36:37] offset1:1
	ds_write_b64 v42, v[46:47] offset:20624

	.amdhsa_kernel _Z7k1_prepPKfPKiPiPfPDF16_S4_
		.amdhsa_group_segment_fixed_size 20704
		.amdhsa_private_segment_fixed_size 0
		.amdhsa_kernarg_size 48
		.amdhsa_user_sgpr_count 2
		.amdhsa_user_sgpr_dispatch_ptr 0
		.amdhsa_user_sgpr_queue_ptr 0
		.amdhsa_user_sgpr_kernarg_segment_ptr 1
		.amdhsa_user_sgpr_dispatch_id 0
		.amdhsa_user_sgpr_kernarg_preload_length 0
		.amdhsa_user_sgpr_kernarg_preload_offset 0
		.amdhsa_user_sgpr_private_segment_size 0
		.amdhsa_uses_dynamic_stack 0
		.amdhsa_enable_private_segment 0
		.amdhsa_system_sgpr_workgroup_id_x 1
		.amdhsa_system_sgpr_workgroup_id_y 0
		.amdhsa_system_sgpr_workgroup_id_z 0
		.amdhsa_system_sgpr_workgroup_info 0
		.amdhsa_system_vgpr_workitem_id 0
		.amdhsa_next_free_vgpr 72
		.amdhsa_next_free_sgpr 75
		.amdhsa_accum_offset 72
		.amdhsa_reserve_vcc 1
		.amdhsa_float_round_mode_32 0
		.amdhsa_float_round_mode_16_64 0
		.amdhsa_float_denorm_mode_32 3
		.amdhsa_float_denorm_mode_16_64 3
		.amdhsa_dx10_clamp 1
		.amdhsa_ieee_mode 1
		.amdhsa_fp16_overflow 0
		.amdhsa_tg_split 0
		.amdhsa_exception_fp_ieee_invalid_op 0
		.amdhsa_exception_fp_denorm_src 0
		.amdhsa_exception_fp_ieee_div_zero 0
		.amdhsa_exception_fp_ieee_overflow 0
		.amdhsa_exception_fp_ieee_underflow 0
		.amdhsa_exception_fp_ieee_inexact 0
		.amdhsa_exception_int_div_zero 0
	.end_amdhsa_kernel

_Z6k3_knnPKiPKfPKDF16_PfS5_S5_:
.Lpf_k3code:
	s_load_dwordx2 s[4:5], s[0:1], 0x0
	s_load_dwordx8 s[60:67], s[0:1], 0x8
	s_load_dwordx2 s[70:71], s[0:1], 0x28
	s_ashr_i32 s3, s2, 31
	s_lshl_b64 s[2:3], s[2:3], 4
	s_waitcnt lgkmcnt(0)
	s_add_u32 s2, s4, s2
	s_addc_u32 s3, s5, s3
	s_load_dwordx4 s[88:91], s[2:3], 0x80
	s_waitcnt lgkmcnt(0)
	s_cmp_lt_i32 s91, 0
	s_cbranch_scc1 .LBB1_46
	s_mov_b32 s77, s91
	v_cvt_f32_ubyte2_e32 v1, s77
	v_rcp_iflag_f32_e32 v1, v1
	s_mov_b32 s58, s89
	s_mov_b32 s59, s90
	s_mov_b32 s4, s88
	s_bfe_u32 s2, s77, 0x80010
	s_sub_i32 s7, 0, s2
	v_mul_f32_e32 v1, 0x4f7ffffe, v1
	v_cvt_u32_f32_e32 v1, v1
	s_waitcnt lgkmcnt(0)
	s_add_i32 s3, s58, 31
	s_ashr_i32 s3, s3, 5
	s_add_i32 s8, s2, -1
	v_readfirstlane_b32 s9, v1
	s_mul_i32 s7, s7, s9
	s_add_i32 s6, s8, s3
	s_mul_hi_u32 s7, s9, s7
	s_and_b32 s76, s77, 0xff
	s_ashr_i32 s5, s6, 31
	s_abs_i32 s6, s6
	s_add_i32 s9, s9, s7
	s_ashr_i32 s72, s4, 5
	s_cmp_eq_u32 s76, s8
	s_mul_hi_u32 s7, s6, s9
	s_cselect_b64 s[68:69], -1, 0
	s_add_i32 s9, s58, 0x7f
	s_ashr_i32 s9, s9, 5
	s_and_b32 s78, s9, -4
	v_lshrrev_b32_e32 v115, 8, v0
	s_cmp_lg_u32 s76, s8
	v_and_b32_e32 v1, 0xff, v0
	v_mov_b32_e32 v109, 0
	v_mov_b32_e32 v120, 0
	v_mov_b32_e32 v121, 0
	v_mov_b32_e32 v122, 0
	v_mov_b32_e32 v123, 0
	v_mov_b32_e32 v124, 0
	v_mov_b32_e32 v125, 0
	v_mov_b32_e32 v126, 0
	v_mov_b32_e32 v127, 0
	v_mov_b32_e32 v128, 0
	v_mov_b32_e32 v129, 0
	v_mov_b32_e32 v130, 0

amdhsa.kernels:
  - .agpr_count:     0
    .args:
      - .actual_access:  read_only
        .address_space:  global
        .offset:         0
        .size:           8
        .value_kind:     global_buffer
      - .actual_access:  read_only
        .address_space:  global
        .offset:         8
        .size:           8
        .value_kind:     global_buffer
      - .actual_access:  write_only
        .address_space:  global
        .offset:         16
        .size:           8
        .value_kind:     global_buffer
      - .actual_access:  write_only
        .address_space:  global
        .offset:         24
        .size:           8
        .value_kind:     global_buffer
      - .actual_access:  write_only
        .address_space:  global
        .offset:         32
        .size:           8
        .value_kind:     global_buffer
      - .actual_access:  write_only
        .address_space:  global
        .offset:         40
        .size:           8
        .value_kind:     global_buffer
    .group_segment_fixed_size: 20704
    .kernarg_segment_align: 8
    .kernarg_segment_size: 48
    .language:       OpenCL C
    .language_version:
      - 2
      - 0
    .max_flat_workgroup_size: 256
    .name:           _Z7k1_prepPKfPKiPiPfPDF16_S4_
    .private_segment_fixed_size: 0
    .sgpr_count:     69
    .sgpr_spill_count: 0
    .symbol:         _Z7k1_prepPKfPKiPiPfPDF16_S4_.kd
    .uniform_work_group_size: 1
    .uses_dynamic_stack: false
    .vgpr_count:     72
    .vgpr_spill_count: 0
    .wavefront_size: 64
  - .agpr_count:     0
    .args:
      - .actual_access:  read_only
        .address_space:  global
        .offset:         0
        .size:           8
        .value_kind:     global_buffer
      - .actual_access:  read_only
        .address_space:  global
        .offset:         8
        .size:           8
        .value_kind:     global_buffer
      - .address_space:  global
        .offset:         16
        .size:           8
        .value_kind:     global_buffer
      - .actual_access:  write_only
        .address_space:  global
        .offset:         24
        .size:           8
        .value_kind:     global_buffer
      - .actual_access:  write_only
        .address_space:  global
        .offset:         32
        .size:           8
        .value_kind:     global_buffer
      - .actual_access:  write_only
        .address_space:  global
        .offset:         40
        .size:           8
        .value_kind:     global_buffer
    .group_segment_fixed_size: 153664
    .kernarg_segment_align: 8
    .kernarg_segment_size: 48
    .language:       OpenCL C
    .language_version:
      - 2
      - 0
    .max_flat_workgroup_size: 768
    .name:           _Z6k3_knnPKiPKfPKDF16_PfS5_S5_
    .private_segment_fixed_size: 0
    .sgpr_count:     92
    .sgpr_spill_count: 0
    .symbol:         _Z6k3_knnPKiPKfPKDF16_PfS5_S5_.kd
    .uniform_work_group_size: 1
    .uses_dynamic_stack: false
    .vgpr_count:     159
    .vgpr_spill_count: 0
    .wavefront_size: 64
  - .agpr_count:     0
    .args:
      - .actual_access:  read_only
        .address_space:  global
        .offset:         0
        .size:           8
        .value_kind:     global_buffer
      - .actual_access:  read_only
        .address_space:  global
        .offset:         8
        .size:           8
        .value_kind:     global_buffer
      - .actual_access:  read_only
        .address_space:  global
        .offset:         16
        .size:           8
        .value_kind:     global_buffer
      - .actual_access:  read_only
        .address_space:  global
        .offset:         24
        .size:           8
        .value_kind:     global_buffer
      - .actual_access:  read_only
        .address_space:  global
        .offset:         32
        .size:           8
        .value_kind:     global_buffer
      - .actual_access:  read_only
        .address_space:  global
        .offset:         40
        .size:           8
        .value_kind:     global_buffer
      - .actual_access:  read_only
        .address_space:  global
        .offset:         48
        .size:           8
        .value_kind:     global_buffer
      - .actual_access:  read_only
        .address_space:  global
        .offset:         56
        .size:           8
        .value_kind:     global_buffer
      - .address_space:  global
        .offset:         64
        .size:           8
        .value_kind:     global_buffer
    .group_segment_fixed_size: 30784
    .kernarg_segment_align: 8
    .kernarg_segment_size: 72
    .language:       OpenCL C
    .language_version:
      - 2
      - 0
    .max_flat_workgroup_size: 1024
    .name:           _Z9k3b_mergePKiPKfS2_S2_S2_S2_S2_S2_Pf
    .private_segment_fixed_size: 0
    .sgpr_count:     56
    .sgpr_spill_count: 0
    .symbol:         _Z9k3b_mergePKiPKfS2_S2_S2_S2_S2_S2_Pf.kd
    .uniform_work_group_size: 1
    .uses_dynamic_stack: false
    .vgpr_count:     70
    .vgpr_spill_count: 0
    .wavefront_size: 64
